# RTO load batching also applied to the ctx-query copy of the retention output unit
# speedup vs baseline: 1.0010x; 1.0010x over previous
.LBB0_1039:
	s_or_b64 exec, exec, s[4:5]
	s_lshl_b32 s0, s9, 3
	s_lshl_b32 s4, s10, 1
	s_or_b32 s0, s4, s0
	s_mul_i32 s0, s0, 18
	s_add_i32 s4, s0, s8
	s_ashr_i32 s5, s4, 31
	s_lshl_b64 s[4:5], s[4:5], 15
	s_add_u32 s4, s12, s4
	s_addc_u32 s5, s13, s5
	v_ashrrev_i32_e32 v147, 2, v143
	v_lshl_add_u64 v[48:49], s[4:5], 0, v[96:97]
	s_movk_i32 s4, 0xffc0
	v_mul_f32_e32 v0, v0, v18
	v_and_or_b32 v60, v147, s4, v16
	v_mul_f32_e32 v1, v1, v19
	v_cvt_pk_bf16_f32 v138, v0, v1
	v_lshlrev_b32_e32 v0, 7, v60
	v_ashrrev_i32_e32 v1, 31, v0
	v_mul_f32_e32 v8, v8, v26
	v_mul_f32_e32 v9, v9, v27
	v_lshlrev_b64 v[26:27], 1, v[0:1]
	v_lshl_add_u64 v[54:55], v[48:49], 0, v[26:27]
	v_mul_f32_e32 v2, v2, v20
	v_mul_f32_e32 v3, v3, v21
	v_mul_f32_e32 v4, v4, v22
	v_mul_f32_e32 v5, v5, v23
	v_mul_f32_e32 v6, v6, v24
	v_mul_f32_e32 v7, v7, v25
	v_mul_f32_e32 v10, v10, v28
	v_mul_f32_e32 v11, v11, v29
	v_mul_f32_e32 v12, v12, v30
	v_mul_f32_e32 v13, v13, v31
	v_mul_f32_e32 v14, v14, v32
	v_mul_f32_e32 v15, v15, v33
	v_cvt_pk_bf16_f32 v139, v2, v3
	v_cvt_pk_bf16_f32 v140, v4, v5
	v_cvt_pk_bf16_f32 v141, v6, v7
	v_cvt_pk_bf16_f32 v134, v8, v9
	v_cvt_pk_bf16_f32 v135, v10, v11
	v_cvt_pk_bf16_f32 v136, v12, v13
	v_cvt_pk_bf16_f32 v137, v14, v15
	global_load_dwordx4 v[160:163], v[54:55], off
	global_load_dwordx4 v[164:167], v[54:55], off offset:32
	global_load_dwordx4 v[168:171], v[54:55], off offset:64
	global_load_dwordx4 v[172:175], v[54:55], off offset:96
	global_load_dwordx4 v[176:179], v[54:55], off offset:128
	global_load_dwordx4 v[180:183], v[54:55], off offset:160
	global_load_dwordx4 v[184:187], v[54:55], off offset:192
	global_load_dwordx4 v[188:191], v[54:55], off offset:224
	s_movk_i32 s11, 0x110
	v_lshlrev_b32_e32 v156, 1, v17
	v_mul_lo_u32 v0, v60, s11
	v_add3_u32 v61, s3, v0, v156
	ds_read2_b64 v[0:3], v61 offset1:2
	ds_read2_b64 v[22:25], v61 offset0:4 offset1:6
	s_waitcnt lgkmcnt(1)
	v_mfma_f32_32x32x16_bf16 v[0:15], v[0:3], v[110:113], 0
	s_sub_i32 s0, s0, s8
	s_add_i32 s0, s0, 19
	s_lshl_b64 s[4:5], s[0:1], 15
	s_add_u32 s4, s12, s4
	s_addc_u32 s5, s13, s5
	v_lshl_add_u64 v[56:57], s[4:5], 0, v[96:97]
	v_lshl_add_u64 v[58:59], v[56:57], 0, v[26:27]
	global_load_dwordx4 v[192:195], v[58:59], off
	global_load_dwordx4 v[196:199], v[58:59], off offset:32
	global_load_dwordx4 v[200:203], v[58:59], off offset:64
	global_load_dwordx4 v[204:207], v[58:59], off offset:96
	global_load_dwordx4 v[208:211], v[58:59], off offset:128
	global_load_dwordx4 v[220:223], v[58:59], off offset:160
	global_load_dwordx4 v[224:227], v[58:59], off offset:192
	global_load_dwordx4 v[228:231], v[58:59], off offset:224
	s_waitcnt lgkmcnt(0)
	v_mfma_f32_32x32x16_bf16 v[0:15], v[22:25], v[114:117], v[0:15]
	ds_read2_b64 v[22:25], v61 offset0:8 offset1:10
	v_or_b32_e32 v157, 32, v60
	v_lshlrev_b32_e32 v54, 7, v157
	v_ashrrev_i32_e32 v55, 31, v54
	v_lshlrev_b64 v[54:55], 1, v[54:55]
	v_lshl_add_u64 v[152:153], v[48:49], 0, v[54:55]
	v_lshl_add_u64 v[154:155], v[56:57], 0, v[54:55]
	global_load_dwordx4 v[232:235], v[152:153], off
	global_load_dwordx4 v[236:239], v[154:155], off
	global_load_dwordx4 v[244:247], v[152:153], off offset:32
	global_load_dwordx4 v[248:251], v[154:155], off offset:32
	global_load_dwordx4 v[214:217], v[152:153], off offset:64
	s_movk_i32 s8, 0x204
	s_lshl_b32 s0, s2, 1
	s_waitcnt lgkmcnt(0)
	v_mfma_f32_32x32x16_bf16 v[0:15], v[22:25], v[122:125], v[0:15]
	s_waitcnt vmcnt(20)
	v_mfma_f32_32x32x16_bf16 v[16:31], v[160:163], v[64:67], 0
	global_load_dwordx4 v[160:163], v[154:155], off offset:64
	s_waitcnt vmcnt(20)
	v_mfma_f32_32x32x16_bf16 v[16:31], v[164:167], v[106:109], v[16:31]
	global_load_dwordx4 v[164:167], v[152:153], off offset:96
	s_waitcnt vmcnt(14)
	v_mfma_f32_32x32x16_bf16 v[32:47], v[192:195], v[64:67], 0
	global_load_dwordx4 v[192:195], v[154:155], off offset:96
	s_waitcnt vmcnt(14)
	v_mfma_f32_32x32x16_bf16 v[32:47], v[196:199], v[106:109], v[32:47]
	global_load_dwordx4 v[196:199], v[152:153], off offset:128
	s_waitcnt vmcnt(22)
	v_mfma_f32_32x32x16_bf16 v[16:31], v[168:171], v[102:105], v[16:31]
	global_load_dwordx4 v[168:171], v[154:155], off offset:128
	s_waitcnt vmcnt(15)
	v_mfma_f32_32x32x16_bf16 v[32:47], v[200:203], v[102:105], v[32:47]
	global_load_dwordx4 v[200:203], v[152:153], off offset:160
	s_waitcnt vmcnt(23)
	v_mfma_f32_32x32x16_bf16 v[16:31], v[172:175], v[92:95], v[16:31]
	global_load_dwordx4 v[172:175], v[154:155], off offset:160
	s_waitcnt vmcnt(16)
	v_mfma_f32_32x32x16_bf16 v[32:47], v[204:207], v[92:95], v[32:47]
	global_load_dwordx4 v[204:207], v[152:153], off offset:192
	s_waitcnt vmcnt(24)
	v_mfma_f32_32x32x16_bf16 v[16:31], v[176:179], v[88:91], v[16:31]
	global_load_dwordx4 v[176:179], v[154:155], off offset:192
	s_waitcnt vmcnt(17)
	v_mfma_f32_32x32x16_bf16 v[32:47], v[208:211], v[88:91], v[32:47]
	global_load_dwordx4 v[208:211], v[152:153], off offset:224
	s_waitcnt vmcnt(25)
	v_mfma_f32_32x32x16_bf16 v[16:31], v[180:183], v[84:87], v[16:31]
	global_load_dwordx4 v[180:183], v[154:155], off offset:224
	s_waitcnt vmcnt(18)
	v_mfma_f32_32x32x16_bf16 v[32:47], v[220:223], v[84:87], v[32:47]
	s_waitcnt vmcnt(25)
	v_mfma_f32_32x32x16_bf16 v[16:31], v[184:187], v[80:83], v[16:31]
	s_waitcnt vmcnt(17)
	v_mfma_f32_32x32x16_bf16 v[32:47], v[224:227], v[80:83], v[32:47]
	s_waitcnt vmcnt(24)
	v_mfma_f32_32x32x16_bf16 v[16:31], v[188:191], v[98:101], v[16:31]
	s_waitcnt vmcnt(16)
	v_mfma_f32_32x32x16_bf16 v[32:47], v[228:231], v[98:101], v[32:47]
	ds_read2_b64 v[50:53], v61 offset0:12 offset1:14
	s_waitcnt lgkmcnt(0)
	v_mfma_f32_32x32x16_bf16 v[0:15], v[50:53], v[118:121], v[0:15]
	ds_read2_b64 v[50:53], v61 offset0:16 offset1:18
	s_waitcnt lgkmcnt(0)
	v_mfma_f32_32x32x16_bf16 v[0:15], v[50:53], v[130:133], v[0:15]
	ds_read2_b64 v[50:53], v61 offset0:20 offset1:22
	s_waitcnt lgkmcnt(0)
	v_mfma_f32_32x32x16_bf16 v[0:15], v[50:53], v[126:129], v[0:15]
	ds_read2_b64 v[50:53], v61 offset0:24 offset1:26
	s_waitcnt lgkmcnt(0)
	v_mfma_f32_32x32x16_bf16 v[0:15], v[50:53], v[138:141], v[0:15]
	ds_read2_b64 v[50:53], v61 offset0:28 offset1:30
	s_waitcnt lgkmcnt(0)
	v_mfma_f32_32x32x16_bf16 v[0:15], v[50:53], v[134:137], v[0:15]
	s_waitcnt vmcnt(15)
	v_mfma_f32_32x32x16_bf16 v[48:63], v[232:235], v[64:67], 0
	s_waitcnt vmcnt(13)
	v_mfma_f32_32x32x16_bf16 v[48:63], v[244:247], v[106:109], v[48:63]
	s_waitcnt vmcnt(14)
	v_mfma_f32_32x32x16_bf16 v[64:79], v[236:239], v[64:67], 0
	s_waitcnt vmcnt(12)
	v_mfma_f32_32x32x16_bf16 v[64:79], v[248:251], v[106:109], v[64:79]
	s_waitcnt vmcnt(11)
	v_mfma_f32_32x32x16_bf16 v[48:63], v[214:217], v[102:105], v[48:63]
	s_waitcnt vmcnt(10)
	v_mfma_f32_32x32x16_bf16 v[64:79], v[160:163], v[102:105], v[64:79]
	s_waitcnt vmcnt(9)
	v_mfma_f32_32x32x16_bf16 v[48:63], v[164:167], v[92:95], v[48:63]
	s_waitcnt vmcnt(8)
	v_mfma_f32_32x32x16_bf16 v[64:79], v[192:195], v[92:95], v[64:79]
	s_waitcnt vmcnt(7)
	v_mfma_f32_32x32x16_bf16 v[48:63], v[196:199], v[88:91], v[48:63]
	s_waitcnt vmcnt(6)
	v_mfma_f32_32x32x16_bf16 v[64:79], v[168:171], v[88:91], v[64:79]
	s_waitcnt vmcnt(5)
	v_mfma_f32_32x32x16_bf16 v[48:63], v[200:203], v[84:87], v[48:63]
	s_waitcnt vmcnt(4)
	v_mfma_f32_32x32x16_bf16 v[64:79], v[172:175], v[84:87], v[64:79]
	s_waitcnt vmcnt(3)
	v_mfma_f32_32x32x16_bf16 v[48:63], v[204:207], v[80:83], v[48:63]
	s_waitcnt vmcnt(2)
	v_mfma_f32_32x32x16_bf16 v[64:79], v[176:179], v[80:83], v[64:79]
	v_mul_lo_u32 v84, v157, s11
	v_add3_u32 v148, s3, v84, v156
	ds_read2_b64 v[106:109], v148 offset0:4 offset1:6
	s_waitcnt vmcnt(1)
	v_mfma_f32_32x32x16_bf16 v[48:63], v[208:211], v[98:101], v[48:63]
	ds_read2_b64 v[80:83], v148 offset1:2
	s_waitcnt lgkmcnt(0)
	v_mfma_f32_32x32x16_bf16 v[80:95], v[80:83], v[110:113], 0
	ds_read2_b64 v[110:113], v148 offset0:12 offset1:14
	v_mfma_f32_32x32x16_bf16 v[80:95], v[106:109], v[114:117], v[80:95]
	ds_read2_b64 v[106:109], v148 offset0:8 offset1:10
	v_add_u32_e32 v114, 1, v146
	s_waitcnt lgkmcnt(0)
	v_mfma_f32_32x32x16_bf16 v[80:95], v[106:109], v[122:125], v[80:95]
	v_cvt_f32_ubyte0_e32 v106, v114
	v_mul_f32_e32 v106, v145, v106
	v_exp_f32_e32 v122, v106
	v_sub_u32_e32 v106, 0x80, v146
	v_cvt_f32_ubyte0_e32 v106, v106
	v_mul_f32_e32 v114, v144, v106
	ds_read2_b64 v[106:109], v148 offset0:16 offset1:18
	v_mfma_f32_32x32x16_bf16 v[80:95], v[110:113], v[118:121], v[80:95]
	v_exp_f32_e32 v124, v114
	ds_read2_b64 v[110:113], v148 offset0:20 offset1:22
	ds_read2_b64 v[114:117], v148 offset0:24 offset1:26
	ds_read2_b64 v[118:121], v148 offset0:28 offset1:30
	v_pk_fma_f32 v[0:1], v[122:123], v[16:17], v[0:1] op_sel_hi:[0,1,1]
	s_waitcnt lgkmcnt(0)
	v_pk_fma_f32 v[0:1], v[124:125], v[32:33], v[0:1] op_sel_hi:[0,1,1]
	s_barrier
	v_mfma_f32_32x32x16_bf16 v[80:95], v[106:109], v[130:133], v[80:95]
	v_mad_u32_u24 v106, v146, s8, 0
	v_and_b32_e32 v107, 0xffffff00, v143
	v_add3_u32 v96, v106, v107, v96
	ds_write2_b32 v96, v0, v1 offset1:1
	v_fma_f32 v0, v122, v18, v2
	v_fma_f32 v1, v122, v19, v3
	v_pk_fma_f32 v[0:1], v[124:125], v[34:35], v[0:1] op_sel_hi:[0,1,1]
	ds_write2_b32 v96, v0, v1 offset0:2 offset1:3
	v_mfma_f32_32x32x16_bf16 v[80:95], v[110:113], v[126:129], v[80:95]
	v_fma_f32 v0, v122, v20, v4
	v_fma_f32 v1, v122, v21, v5
	v_fma_f32 v0, v124, v36, v0
	v_fma_f32 v1, v124, v37, v1
	ds_write2_b32 v96, v0, v1 offset0:8 offset1:9
	v_pk_fma_f32 v[0:1], v[122:123], v[22:23], v[6:7] op_sel_hi:[0,1,1]
	v_pk_fma_f32 v[0:1], v[124:125], v[38:39], v[0:1] op_sel_hi:[0,1,1]
	ds_write2_b32 v96, v0, v1 offset0:10 offset1:11
	v_pk_fma_f32 v[0:1], v[122:123], v[24:25], v[8:9] op_sel_hi:[0,1,1]
	v_mfma_f32_32x32x16_bf16 v[80:95], v[114:117], v[138:141], v[80:95]
	v_fma_f32 v0, v124, v40, v0
	v_fma_f32 v1, v124, v41, v1
	ds_write2_b32 v96, v0, v1 offset0:16 offset1:17
	v_fma_f32 v0, v122, v26, v10
	v_fma_f32 v1, v122, v27, v11
	v_pk_fma_f32 v[0:1], v[124:125], v[42:43], v[0:1] op_sel_hi:[0,1,1]
	ds_write2_b32 v96, v0, v1 offset0:18 offset1:19
	v_pk_fma_f32 v[0:1], v[122:123], v[28:29], v[12:13] op_sel_hi:[0,1,1]
	v_pk_fma_f32 v[0:1], v[124:125], v[44:45], v[0:1] op_sel_hi:[0,1,1]
	v_mfma_f32_32x32x16_bf16 v[80:95], v[118:121], v[134:137], v[80:95]
	ds_write2_b32 v96, v0, v1 offset0:24 offset1:25
	v_fma_f32 v0, v122, v30, v14
	v_fma_f32 v1, v122, v31, v15
	v_fma_f32 v0, v124, v46, v0
	v_fma_f32 v1, v124, v47, v1
	ds_write2_b32 v96, v0, v1 offset0:26 offset1:27
	v_add_u32_e32 v36, s7, v147
	v_and_b32_e32 v2, 3, v142
	s_nop 3
	v_pk_fma_f32 v[0:1], v[122:123], v[48:49], v[80:81] op_sel_hi:[0,1,1]
	s_waitcnt vmcnt(0)
	v_mfma_f32_32x32x16_bf16 v[64:79], v[180:183], v[98:101], v[64:79]
	s_nop 11
	v_pk_fma_f32 v[0:1], v[124:125], v[64:65], v[0:1] op_sel_hi:[0,1,1]
	ds_write2_b32 v96, v0, v1 offset0:32 offset1:33
	v_pk_fma_f32 v[0:1], v[122:123], v[50:51], v[82:83] op_sel_hi:[0,1,1]
	v_pk_fma_f32 v[0:1], v[124:125], v[66:67], v[0:1] op_sel_hi:[0,1,1]
	ds_write2_b32 v96, v0, v1 offset0:34 offset1:35
	v_pk_fma_f32 v[0:1], v[122:123], v[52:53], v[84:85] op_sel_hi:[0,1,1]
	v_pk_fma_f32 v[0:1], v[124:125], v[68:69], v[0:1] op_sel_hi:[0,1,1]
	ds_write2_b32 v96, v0, v1 offset0:40 offset1:41
	v_pk_fma_f32 v[0:1], v[122:123], v[54:55], v[86:87] op_sel_hi:[0,1,1]
	v_pk_fma_f32 v[0:1], v[124:125], v[70:71], v[0:1] op_sel_hi:[0,1,1]
	ds_write2_b32 v96, v0, v1 offset0:42 offset1:43
	v_pk_fma_f32 v[0:1], v[122:123], v[56:57], v[88:89] op_sel_hi:[0,1,1]
	v_pk_fma_f32 v[0:1], v[124:125], v[72:73], v[0:1] op_sel_hi:[0,1,1]
	ds_write2_b32 v96, v0, v1 offset0:48 offset1:49
	v_pk_fma_f32 v[0:1], v[122:123], v[58:59], v[90:91] op_sel_hi:[0,1,1]
	v_pk_fma_f32 v[0:1], v[124:125], v[74:75], v[0:1] op_sel_hi:[0,1,1]
	ds_write2_b32 v96, v0, v1 offset0:50 offset1:51
	v_pk_fma_f32 v[0:1], v[122:123], v[60:61], v[92:93] op_sel_hi:[0,1,1]
	v_pk_fma_f32 v[0:1], v[124:125], v[76:77], v[0:1] op_sel_hi:[0,1,1]
	ds_write2_b32 v96, v0, v1 offset0:56 offset1:57
	v_pk_fma_f32 v[0:1], v[122:123], v[62:63], v[94:95] op_sel_hi:[0,1,1]
	v_pk_fma_f32 v[0:1], v[124:125], v[78:79], v[0:1] op_sel_hi:[0,1,1]
	ds_write2_b32 v96, v0, v1 offset0:58 offset1:59
	v_mov_b64_e32 v[0:1], s[84:85]
	v_mad_i64_i32 v[0:1], s[4:5], v36, s95, v[0:1]
	v_lshl_add_u64 v[0:1], v[0:1], 0, s[0:1]
	v_lshlrev_b32_e32 v96, 6, v2
	v_lshl_add_u64 v[10:11], v[0:1], 0, v[96:97]
	v_add_co_u32_e32 v0, vcc, s63, v10
	s_waitcnt lgkmcnt(0)
	s_nop 0
	v_addc_co_u32_e32 v1, vcc, 0, v11, vcc
	s_barrier
	global_load_dwordx4 v[24:27], v[0:1], off offset:2048
	v_mul_lo_u32 v0, v147, s8
	v_readlane_b32 s8, v255, 1
	v_lshlrev_b32_e32 v54, 7, v2
	v_readlane_b32 s9, v255, 2
	v_add3_u32 v0, 0, v0, v54
	ds_read2_b32 v[38:39], v0 offset1:1
	s_mov_b64 s[4:5], 0x1800
	v_lshl_add_u64 v[10:11], v[10:11], 0, s[4:5]
	s_mov_b64 s[4:5], 0x18b00400
	global_load_dwordx4 v[28:31], v54, s[8:9]
	global_load_dwordx4 v[32:35], v54, s[8:9] offset:16
	ds_read2_b32 v[40:41], v0 offset0:2 offset1:3
	ds_read2_b32 v[42:43], v0 offset0:4 offset1:5
	ds_read2_b32 v[44:45], v0 offset0:6 offset1:7
	s_waitcnt lgkmcnt(3)
	v_mul_f32_e32 v37, v39, v39
	v_fmac_f32_e32 v37, v38, v38
	s_waitcnt lgkmcnt(2)
	v_fmac_f32_e32 v37, v40, v40
	v_fmac_f32_e32 v37, v41, v41
	ds_read2_b32 v[46:47], v0 offset0:8 offset1:9
	s_waitcnt lgkmcnt(2)
	v_fmac_f32_e32 v37, v42, v42
	v_fmac_f32_e32 v37, v43, v43
	s_waitcnt lgkmcnt(1)
	v_fmac_f32_e32 v37, v44, v44
	v_fmac_f32_e32 v37, v45, v45
	ds_read2_b32 v[48:49], v0 offset0:10 offset1:11
	ds_read2_b32 v[20:21], v0 offset0:12 offset1:13
	ds_read2_b32 v[18:19], v0 offset0:14 offset1:15
	s_waitcnt lgkmcnt(3)
	v_fmac_f32_e32 v37, v46, v46
	v_fmac_f32_e32 v37, v47, v47
	s_waitcnt lgkmcnt(2)
	v_fmac_f32_e32 v37, v48, v48
	v_fmac_f32_e32 v37, v49, v49
	ds_read2_b32 v[16:17], v0 offset0:16 offset1:17
	s_waitcnt lgkmcnt(2)
	v_fmac_f32_e32 v37, v20, v20
	v_fmac_f32_e32 v37, v21, v21
	s_waitcnt lgkmcnt(1)
	v_fmac_f32_e32 v37, v18, v18
	v_fmac_f32_e32 v37, v19, v19
	ds_read2_b32 v[14:15], v0 offset0:18 offset1:19
	ds_read2_b32 v[12:13], v0 offset0:20 offset1:21
	ds_read2_b32 v[8:9], v0 offset0:22 offset1:23
	s_waitcnt lgkmcnt(3)
	v_fmac_f32_e32 v37, v16, v16
	v_fmac_f32_e32 v37, v17, v17
	s_waitcnt lgkmcnt(2)
	v_fmac_f32_e32 v37, v14, v14
	ds_read2_b32 v[6:7], v0 offset0:24 offset1:25
	v_fmac_f32_e32 v37, v15, v15
	s_waitcnt lgkmcnt(2)
	v_fmac_f32_e32 v37, v12, v12
	v_fmac_f32_e32 v37, v13, v13
	s_waitcnt lgkmcnt(1)
	v_fmac_f32_e32 v37, v8, v8
	ds_read2_b32 v[4:5], v0 offset0:26 offset1:27
	ds_read2_b32 v[2:3], v0 offset0:28 offset1:29
	ds_read2_b32 v[0:1], v0 offset0:30 offset1:31
	v_fmac_f32_e32 v37, v9, v9
	s_waitcnt lgkmcnt(3)
	v_pk_mul_f32 v[22:23], v[6:7], v[6:7]
	s_waitcnt vmcnt(2)
	v_lshlrev_b32_e32 v50, 16, v24
	v_add_f32_e32 v22, v37, v22
	v_add_f32_e32 v37, v22, v23
	s_waitcnt lgkmcnt(2)
	v_pk_mul_f32 v[22:23], v[4:5], v[4:5]
	s_waitcnt vmcnt(1)
	v_mov_b32_e32 v53, v28
	v_add_f32_e32 v22, v37, v22
	v_add_f32_e32 v37, v22, v23
	s_waitcnt lgkmcnt(1)
	v_pk_mul_f32 v[22:23], v[2:3], v[2:3]
	s_nop 0
	v_add_f32_e32 v22, v37, v22
	v_add_f32_e32 v37, v22, v23
	s_waitcnt lgkmcnt(0)
	v_pk_mul_f32 v[22:23], v[0:1], v[0:1]
	s_nop 0
	v_add_f32_e32 v22, v37, v22
	v_add_f32_e32 v22, v22, v23
	v_ashrrev_i32_e32 v37, 31, v36
	v_lshlrev_b64 v[36:37], 12, v[36:37]
	v_add_f32_dpp v22, v22, v22 quad_perm:[1,0,3,2] row_mask:0xf bank_mask:0xf bound_ctrl:1
	v_lshl_add_u64 v[36:37], s[96:97], 0, v[36:37]
	s_nop 0
	v_add_f32_dpp v22, v22, v22 quad_perm:[2,3,0,1] row_mask:0xf bank_mask:0xf bound_ctrl:1
	v_fmamk_f32 v22, v22, 0x3c000000, v213
	v_mul_f32_e32 v23, 0x4b800000, v22
	v_cmp_gt_f32_e32 vcc, s64, v22
	s_nop 1
	v_cndmask_b32_e32 v22, v22, v23, vcc
	v_rsq_f32_e32 v22, v22
	s_nop 0
	v_mul_f32_e32 v23, 0x45800000, v22
	v_cndmask_b32_e32 v22, v22, v23, vcc
	v_mul_f32_e32 v51, v38, v22
	v_mul_f32_e32 v23, 0xbfb8aa3b, v50
	v_and_b32_e32 v38, 0xffff0000, v24
	v_exp_f32_e32 v23, v23
	v_mul_f32_e32 v24, 0xbfb8aa3b, v38
	v_exp_f32_e32 v24, v24
	v_mul_f32_e32 v39, v39, v22
	v_add_f32_e32 v23, 1.0, v23
	v_rcp_f32_e32 v52, v23
	v_add_f32_e32 v23, 1.0, v24
	v_rcp_f32_e32 v28, v23
	v_mul_f32_e32 v19, v19, v22
	v_pk_mul_f32 v[50:51], v[52:53], v[50:51]
	v_mul_f32_e32 v9, v9, v22
	v_pk_mul_f32 v[28:29], v[28:29], v[38:39]
	v_mul_f32_e32 v23, v50, v51
	v_mul_f32_e32 v50, v28, v29
	v_lshlrev_b32_e32 v28, 16, v25
	v_mul_f32_e32 v24, 0xbfb8aa3b, v28
	v_exp_f32_e32 v38, v24
	v_and_b32_e32 v24, 0xffff0000, v25
	v_mul_f32_e32 v25, 0xbfb8aa3b, v24
	v_exp_f32_e32 v25, v25
	v_add_f32_e32 v38, 1.0, v38
	v_mov_b32_e32 v39, v30
	v_rcp_f32_e32 v38, v38
	v_add_f32_e32 v25, 1.0, v25
	v_rcp_f32_e32 v30, v25
	v_mul_f32_e32 v25, v41, v22
	v_mul_f32_e32 v29, v40, v22
	v_pk_mul_f32 v[28:29], v[38:39], v[28:29]
	v_pk_mul_f32 v[24:25], v[30:31], v[24:25]
	v_mul_f32_e32 v38, v28, v29
	v_mul_f32_e32 v39, v24, v25
	v_lshlrev_b32_e32 v24, 16, v26
	v_mul_f32_e32 v28, 0xbfb8aa3b, v24
	v_exp_f32_e32 v29, v28
	v_and_b32_e32 v28, 0xffff0000, v26
	v_mul_f32_e32 v26, 0xbfb8aa3b, v28
	v_exp_f32_e32 v26, v26
	v_add_f32_e32 v29, 1.0, v29
	v_rcp_f32_e32 v30, v29
	s_waitcnt vmcnt(0)
	v_mov_b32_e32 v31, v32
	v_add_f32_e32 v26, 1.0, v26
	v_rcp_f32_e32 v32, v26
	v_mul_f32_e32 v25, v42, v22
	v_pk_mul_f32 v[24:25], v[30:31], v[24:25]
	v_mul_f32_e32 v29, v43, v22
	v_mul_f32_e32 v30, v24, v25
	v_pk_mul_f32 v[24:25], v[32:33], v[28:29]
	v_mov_b32_e32 v29, v34
	v_mul_f32_e32 v31, v24, v25
	v_lshlrev_b32_e32 v24, 16, v27
	v_mul_f32_e32 v26, 0xbfb8aa3b, v24
	v_exp_f32_e32 v28, v26
	v_and_b32_e32 v26, 0xffff0000, v27
	v_mul_f32_e32 v27, 0xbfb8aa3b, v26
	v_exp_f32_e32 v27, v27
	v_add_f32_e32 v28, 1.0, v28
	v_rcp_f32_e32 v28, v28
	v_mul_f32_e32 v25, v44, v22
	v_add_f32_e32 v27, 1.0, v27
	v_rcp_f32_e32 v34, v27
	v_pk_mul_f32 v[24:25], v[28:29], v[24:25]
	v_mul_f32_e32 v27, v45, v22
	v_mul_f32_e32 v28, v24, v25
	v_pk_mul_f32 v[24:25], v[34:35], v[26:27]
	v_lshl_add_u64 v[32:33], v[36:37], 0, s[0:1]
	v_mul_f32_e32 v27, v24, v25
	v_cvt_pk_bf16_f32 v24, v23, v50
	v_cvt_pk_bf16_f32 v25, v38, v39
	v_cvt_pk_bf16_f32 v26, v30, v31
	v_cvt_pk_bf16_f32 v27, v28, v27
	global_load_dwordx4 v[28:31], v[10:11], off offset:16
	v_lshl_add_u64 v[36:37], v[32:33], 0, v[96:97]
	s_mov_b32 s0, 0x18b00000
	v_add_co_u32_e32 v32, vcc, s0, v36
	v_mul_f32_e32 v40, v46, v22
	s_nop 0
	v_addc_co_u32_e32 v33, vcc, 0, v37, vcc
	global_store_dwordx4 v[32:33], v[24:27], off offset:1024
	global_load_dwordx4 v[24:27], v54, s[8:9] offset:32
	s_nop 0
	global_load_dwordx4 v[32:35], v54, s[8:9] offset:48
	v_mul_f32_e32 v1, v1, v22
	s_waitcnt vmcnt(3)
	v_lshlrev_b32_e32 v39, 16, v28
	v_mul_f32_e32 v23, 0xbfb8aa3b, v39
	v_exp_f32_e32 v23, v23
	v_and_b32_e32 v43, 0xffff0000, v28
	v_add_f32_e32 v23, 1.0, v23
	v_rcp_f32_e32 v41, v23
	v_mul_f32_e32 v23, 0xbfb8aa3b, v43
	v_exp_f32_e32 v23, v23
	s_waitcnt vmcnt(1)
	v_mov_b32_e32 v38, v24
	v_pk_mul_f32 v[38:39], v[40:41], v[38:39]
	v_mov_b32_e32 v42, v25
	v_add_f32_e32 v23, 1.0, v23
	v_lshlrev_b32_e32 v25, 16, v29
	v_mul_f32_e32 v40, v38, v39
	v_rcp_f32_e32 v39, v23
	v_mul_f32_e32 v23, 0xbfb8aa3b, v25
	v_exp_f32_e32 v23, v23
	v_mul_f32_e32 v38, v47, v22
	v_pk_mul_f32 v[38:39], v[38:39], v[42:43]
	v_and_b32_e32 v29, 0xffff0000, v29
	v_add_f32_e32 v23, 1.0, v23
	v_mul_f32_e32 v41, v38, v39
	v_rcp_f32_e32 v39, v23
	v_mul_f32_e32 v23, 0xbfb8aa3b, v29
	v_exp_f32_e32 v23, v23
	v_mul_f32_e32 v38, v48, v22
	v_mov_b32_e32 v24, v26
	v_pk_mul_f32 v[24:25], v[38:39], v[24:25]
	v_add_f32_e32 v23, 1.0, v23
	v_lshlrev_b32_e32 v39, 16, v30
	v_mul_f32_e32 v42, v24, v25
	v_rcp_f32_e32 v25, v23
	v_mul_f32_e32 v23, 0xbfb8aa3b, v39
	v_exp_f32_e32 v23, v23
	v_mul_f32_e32 v24, v49, v22
	v_mov_b32_e32 v28, v27
	v_pk_mul_f32 v[24:25], v[24:25], v[28:29]
	v_add_f32_e32 v23, 1.0, v23
	v_and_b32_e32 v27, 0xffff0000, v30
	v_mul_f32_e32 v43, v24, v25
	v_rcp_f32_e32 v25, v23
	v_mul_f32_e32 v23, 0xbfb8aa3b, v27
	v_exp_f32_e32 v23, v23
	v_mul_f32_e32 v24, v20, v22
	v_mul_f32_e32 v28, v21, v22
	s_waitcnt vmcnt(0)
	v_mov_b32_e32 v26, v33
	v_add_f32_e32 v20, 1.0, v23
	v_rcp_f32_e32 v29, v20
	v_mov_b32_e32 v38, v32
	v_pk_mul_f32 v[24:25], v[24:25], v[38:39]
	v_pk_mul_f32 v[20:21], v[28:29], v[26:27]
	s_nop 0
	v_mul_f32_e32 v26, v20, v21
	v_lshlrev_b32_e32 v20, 16, v31
	v_mul_f32_e32 v21, 0xbfb8aa3b, v20
	v_mul_f32_e32 v23, v24, v25
	v_exp_f32_e32 v24, v21
	v_mov_b32_e32 v21, v34
	v_and_b32_e32 v34, 0xffff0000, v31
	v_mul_f32_e32 v25, 0xbfb8aa3b, v34
	v_exp_f32_e32 v27, v25
	v_add_f32_e32 v24, 1.0, v24
	v_mul_f32_e32 v25, v18, v22
	v_rcp_f32_e32 v24, v24
	v_add_f32_e32 v18, 1.0, v27
	v_rcp_f32_e32 v18, v18
	v_pk_mul_f32 v[20:21], v[24:25], v[20:21]
	s_nop 0
	v_mul_f32_e32 v20, v20, v21
	v_pk_mul_f32 v[18:19], v[18:19], v[34:35]
	v_cvt_pk_bf16_f32 v24, v40, v41
	v_cvt_pk_bf16_f32 v25, v42, v43
	v_cvt_pk_bf16_f32 v26, v23, v26
	s_nop 0
	v_mul_f32_e32 v18, v18, v19
	v_cvt_pk_bf16_f32 v27, v20, v18
	global_load_dwordx4 v[28:31], v[10:11], off offset:32
	v_lshl_add_u64 v[18:19], v[36:37], 0, s[4:5]
	global_store_dwordx4 v[18:19], v[24:27], off offset:16
	global_load_dwordx4 v[24:27], v54, s[8:9] offset:64
	s_nop 0
	global_load_dwordx4 v[32:35], v54, s[8:9] offset:80
	v_mul_f32_e32 v36, v16, v22
	v_readlane_b32 s4, v254, 49
	s_add_i32 s6, s6, s4
	s_cmp_lt_i32 s6, 64
	v_readlane_b32 s5, v254, 50
	s_waitcnt vmcnt(3)
	v_lshlrev_b32_e32 v21, 16, v28
	v_mul_f32_e32 v20, 0xbfb8aa3b, v21
	v_exp_f32_e32 v20, v20
	v_and_b32_e32 v39, 0xffff0000, v28
	s_waitcnt vmcnt(1)
	v_mov_b32_e32 v38, v25
	v_and_b32_e32 v25, 0xffff0000, v29
	v_add_f32_e32 v16, 1.0, v20
	v_rcp_f32_e32 v37, v16
	v_mul_f32_e32 v16, 0xbfb8aa3b, v39
	v_exp_f32_e32 v23, v16
	v_mov_b32_e32 v20, v24
	v_pk_mul_f32 v[20:21], v[36:37], v[20:21]
	v_mul_f32_e32 v16, v17, v22
	v_mul_f32_e32 v28, v20, v21
	v_add_f32_e32 v17, 1.0, v23
	v_lshlrev_b32_e32 v21, 16, v29
	v_rcp_f32_e32 v17, v17
	v_mul_f32_e32 v20, 0xbfb8aa3b, v21
	v_exp_f32_e32 v20, v20
	v_pk_mul_f32 v[16:17], v[16:17], v[38:39]
	s_nop 0
	v_mul_f32_e32 v23, v16, v17
	v_mul_f32_e32 v16, v14, v22
	v_add_f32_e32 v14, 1.0, v20
	v_rcp_f32_e32 v17, v14
	v_mul_f32_e32 v14, 0xbfb8aa3b, v25
	v_exp_f32_e32 v24, v14
	v_mov_b32_e32 v20, v26
	v_pk_mul_f32 v[16:17], v[16:17], v[20:21]
	v_mul_f32_e32 v14, v15, v22
	v_mul_f32_e32 v26, v16, v17
	v_add_f32_e32 v15, 1.0, v24
	v_lshlrev_b32_e32 v17, 16, v30
	v_rcp_f32_e32 v15, v15
	v_mul_f32_e32 v16, 0xbfb8aa3b, v17
	v_exp_f32_e32 v16, v16
	v_mov_b32_e32 v24, v27
	v_pk_mul_f32 v[14:15], v[14:15], v[24:25]
	v_and_b32_e32 v21, 0xffff0000, v30
	v_mul_f32_e32 v24, v14, v15
	v_add_f32_e32 v14, 1.0, v16
	v_rcp_f32_e32 v15, v14
	v_mul_f32_e32 v14, 0xbfb8aa3b, v21
	v_exp_f32_e32 v20, v14
	v_mul_f32_e32 v14, v12, v22
	s_waitcnt vmcnt(0)
	v_mov_b32_e32 v16, v32
	v_pk_mul_f32 v[14:15], v[14:15], v[16:17]
	v_add_f32_e32 v12, 1.0, v20
	v_rcp_f32_e32 v17, v12
	v_mul_f32_e32 v16, v13, v22
	v_mov_b32_e32 v20, v33
	v_mul_f32_e32 v25, v14, v15
	v_pk_mul_f32 v[12:13], v[16:17], v[20:21]
	v_mul_f32_e32 v20, v6, v22
	v_mul_f32_e32 v16, v12, v13
	v_lshlrev_b32_e32 v12, 16, v31
	v_mul_f32_e32 v13, 0xbfb8aa3b, v12
	v_exp_f32_e32 v14, v13
	v_mov_b32_e32 v13, v34
	v_and_b32_e32 v34, 0xffff0000, v31
	v_mul_f32_e32 v15, 0xbfb8aa3b, v34
	v_exp_f32_e32 v17, v15
	v_add_f32_e32 v14, 1.0, v14
	v_mul_f32_e32 v15, v8, v22
	v_rcp_f32_e32 v14, v14
	v_add_f32_e32 v8, 1.0, v17
	v_rcp_f32_e32 v8, v8
	v_pk_mul_f32 v[12:13], v[14:15], v[12:13]
	s_nop 0
	v_mul_f32_e32 v15, v12, v13
	v_pk_mul_f32 v[8:9], v[8:9], v[34:35]
	v_cvt_pk_bf16_f32 v12, v28, v23
	v_cvt_pk_bf16_f32 v13, v26, v24
	v_cvt_pk_bf16_f32 v14, v25, v16
	s_nop 0
	v_mul_f32_e32 v8, v8, v9
	v_cvt_pk_bf16_f32 v15, v15, v8
	global_load_dwordx4 v[8:11], v[10:11], off offset:48
	s_waitcnt vmcnt(0)
	v_lshlrev_b32_e32 v17, 16, v8
	global_store_dwordx4 v[18:19], v[12:15], off offset:32
	global_load_dwordx4 v[12:15], v54, s[8:9] offset:96
	s_nop 0
	global_load_dwordx4 v[24:27], v54, s[8:9] offset:112
	v_mul_f32_e32 v16, 0xbfb8aa3b, v17
	v_exp_f32_e32 v16, v16
	v_and_b32_e32 v29, 0xffff0000, v8
	v_add_f32_e32 v6, 1.0, v16
	v_rcp_f32_e32 v21, v6
	v_mul_f32_e32 v6, 0xbfb8aa3b, v29
	v_exp_f32_e32 v8, v6
	v_mul_f32_e32 v6, v7, v22
	v_add_f32_e32 v7, 1.0, v8
	v_rcp_f32_e32 v7, v7
	s_waitcnt vmcnt(1)
	v_mov_b32_e32 v28, v13
	v_lshlrev_b32_e32 v13, 16, v9
	v_mul_f32_e32 v8, 0xbfb8aa3b, v13
	v_exp_f32_e32 v8, v8
	v_mov_b32_e32 v16, v12
	v_pk_mul_f32 v[16:17], v[20:21], v[16:17]
	v_pk_mul_f32 v[6:7], v[6:7], v[28:29]
	v_mul_f32_e32 v16, v16, v17
	v_mul_f32_e32 v17, v6, v7
	v_mul_f32_e32 v6, v4, v22
	v_add_f32_e32 v4, 1.0, v8
	v_and_b32_e32 v9, 0xffff0000, v9
	v_rcp_f32_e32 v7, v4
	v_mul_f32_e32 v4, 0xbfb8aa3b, v9
	v_exp_f32_e32 v8, v4
	v_mov_b32_e32 v12, v14
	v_pk_mul_f32 v[6:7], v[6:7], v[12:13]
	v_mul_f32_e32 v4, v5, v22
	v_mul_f32_e32 v12, v6, v7
	v_add_f32_e32 v5, 1.0, v8
	v_lshlrev_b32_e32 v7, 16, v10
	v_rcp_f32_e32 v5, v5
	v_mul_f32_e32 v6, 0xbfb8aa3b, v7
	v_exp_f32_e32 v6, v6
	v_mov_b32_e32 v8, v15
	v_pk_mul_f32 v[4:5], v[4:5], v[8:9]
	v_and_b32_e32 v9, 0xffff0000, v10
	v_mul_f32_e32 v13, v4, v5
	v_add_f32_e32 v4, 1.0, v6
	v_rcp_f32_e32 v5, v4
	v_mul_f32_e32 v4, 0xbfb8aa3b, v9
	v_exp_f32_e32 v8, v4
	v_mul_f32_e32 v4, v2, v22
	s_waitcnt vmcnt(0)
	v_mov_b32_e32 v6, v24
	v_pk_mul_f32 v[4:5], v[4:5], v[6:7]
	v_add_f32_e32 v2, 1.0, v8
	v_rcp_f32_e32 v7, v2
	v_mul_f32_e32 v6, v3, v22
	v_mov_b32_e32 v8, v25
	v_mul_f32_e32 v10, v4, v5
	v_pk_mul_f32 v[2:3], v[6:7], v[8:9]
	s_nop 0
	v_mul_f32_e32 v6, v2, v3
	v_lshlrev_b32_e32 v2, 16, v11
	v_mul_f32_e32 v3, 0xbfb8aa3b, v2
	v_exp_f32_e32 v4, v3
	v_mov_b32_e32 v3, v26
	v_and_b32_e32 v26, 0xffff0000, v11
	v_mul_f32_e32 v5, 0xbfb8aa3b, v26
	v_exp_f32_e32 v7, v5
	v_add_f32_e32 v4, 1.0, v4
	v_rcp_f32_e32 v4, v4
	v_mul_f32_e32 v5, v0, v22
	v_add_f32_e32 v0, 1.0, v7
	v_rcp_f32_e32 v0, v0
	v_pk_mul_f32 v[2:3], v[4:5], v[2:3]
	v_pk_mul_f32 v[0:1], v[0:1], v[26:27]
	v_mul_f32_e32 v3, v2, v3
	v_mul_f32_e32 v4, v0, v1
	v_cvt_pk_bf16_f32 v0, v16, v17
	v_cvt_pk_bf16_f32 v1, v12, v13
	v_cvt_pk_bf16_f32 v2, v10, v6
	v_cvt_pk_bf16_f32 v3, v3, v4
	global_store_dwordx4 v[18:19], v[0:3], off offset:48
	s_barrier
	s_cbranch_scc0 .LBB0_993
.LBB0_1040:
	s_getreg_b32 s0, hwreg(HW_REG_HW_ID, 0, 6)
	s_and_b32 s0, s0, 63
	s_lshl_b32 s0, s0, 2
	s_add_i32 s0, s0, 0
	s_add_i32 s0, s0, 0x20010
	v_mov_b32_e32 v0, s0
	ds_read_b32 v0, v0
	s_and_b32 s9, s6, 7
	s_ashr_i32 s8, s6, 5
	s_bfe_u32 s10, s6, 0x20003
	s_lshl_b32 s2, s9, 8
	s_lshl_b32 s4, s8, 7
	s_add_i32 s7, s4, s2
	s_lshl_b32 s2, s10, 2
	s_waitcnt lgkmcnt(0)
	v_readfirstlane_b32 s0, v0
	v_mov_b32_e32 v0, s2
	s_waitcnt vmcnt(2)
	v_mbcnt_lo_u32_b32 v142, -1, 0
	v_mbcnt_hi_u32_b32 v142, -1, v142
	global_load_dword v145, v0, s[44:45] offset:32
	global_load_dword v144, v0, s[44:45] offset:48
	v_lshlrev_b32_e32 v0, 4, v142
	s_lshl_b32 s0, s0, 6
	v_and_b32_e32 v96, 0xf0, v0
	v_mov_b32_e32 v0, 0x7f
	s_addk_i32 s7, 0x4000
	v_bitop3_b32 v6, s0, v0, v142 bitop3:0xc8
	v_or_b32_e32 v143, s0, v142
	v_or_b32_e32 v0, s7, v6
	v_mov_b64_e32 v[4:5], s[84:85]
	v_mad_i64_i32 v[0:1], s[4:5], v0, s95, v[4:5]
	s_lshl_b32 s0, s10, 8
	s_waitcnt vmcnt(2)
	v_ashrrev_i32_e32 v17, 4, v143
	v_lshl_add_u64 v[0:1], v[0:1], 0, s[0:1]
	s_mov_b64 s[4:5], 0x1400
	v_add_u32_e32 v8, s7, v17
	v_lshl_add_u64 v[0:1], v[0:1], 0, s[4:5]
	v_mad_i64_i32 v[8:9], s[4:5], v8, s95, v[4:5]
	v_lshl_add_u64 v[8:9], v[8:9], 0, s[0:1]
	v_lshl_add_u64 v[12:13], v[8:9], 0, v[96:97]
	s_barrier
	v_bfe_u32 v3, v142, 5, 1
	v_add_u32_e32 v2, 0, v96
	v_lshlrev_b32_e32 v6, 1, v6
	v_add_u32_e32 v7, s3, v6
	v_and_b32_e32 v16, 31, v142
	global_load_dwordx4 v[20:23], v[12:13], off offset:3072
	v_add_co_u32_e32 v8, vcc, s63, v12
	s_nop 1
	v_addc_co_u32_e32 v9, vcc, 0, v13, vcc
	global_load_dwordx4 v[24:27], v[8:9], off
	v_mad_u32_u24 v72, v17, s11, v2
	v_and_b32_e32 v8, -8, v17
	v_ashrrev_i32_e32 v9, 31, v8
	v_lshl_add_u64 v[10:11], v[8:9], 1, v[0:1]
	global_load_dwordx4 v[28:31], v[10:11], off
	v_mul_lo_u32 v8, v8, s11
	v_add_u32_e32 v76, v7, v8
	v_add_u32_e32 v8, 0x200, v143
	v_ashrrev_i32_e32 v14, 4, v8
	v_add_u32_e32 v8, s7, v14
	v_mad_i64_i32 v[8:9], s[4:5], v8, s95, v[4:5]
	v_lshl_add_u64 v[8:9], v[8:9], 0, s[0:1]
	v_lshl_add_u64 v[12:13], v[8:9], 0, v[96:97]
	global_load_dwordx4 v[32:35], v[12:13], off offset:3072
	v_add_co_u32_e32 v8, vcc, s63, v12
	s_nop 1
	v_addc_co_u32_e32 v9, vcc, 0, v13, vcc
	global_load_dwordx4 v[36:39], v[8:9], off
	v_mad_u32_u24 v73, v14, s11, v2
	v_and_b32_e32 v8, -8, v14
	v_ashrrev_i32_e32 v9, 31, v8
	v_lshl_add_u64 v[10:11], v[8:9], 1, v[0:1]
	global_load_dwordx4 v[40:43], v[10:11], off
	v_mul_lo_u32 v8, v8, s11
	v_add_u32_e32 v77, v7, v8
	v_add_u32_e32 v8, 0x400, v143
	v_ashrrev_i32_e32 v14, 4, v8
	v_add_u32_e32 v8, s7, v14
	v_mad_i64_i32 v[8:9], s[4:5], v8, s95, v[4:5]
	v_lshl_add_u64 v[8:9], v[8:9], 0, s[0:1]
	v_lshl_add_u64 v[12:13], v[8:9], 0, v[96:97]
	global_load_dwordx4 v[44:47], v[12:13], off offset:3072
	v_add_co_u32_e32 v8, vcc, s63, v12
	s_nop 1
	v_addc_co_u32_e32 v9, vcc, 0, v13, vcc
	global_load_dwordx4 v[48:51], v[8:9], off
	v_mad_u32_u24 v74, v14, s11, v2
	v_and_b32_e32 v8, -8, v14
	v_ashrrev_i32_e32 v9, 31, v8
	v_lshl_add_u64 v[10:11], v[8:9], 1, v[0:1]
	global_load_dwordx4 v[52:55], v[10:11], off
	v_mul_lo_u32 v8, v8, s11
	v_add_u32_e32 v78, v7, v8
	v_add_u32_e32 v8, 0x600, v143
	v_ashrrev_i32_e32 v14, 4, v8
	v_add_u32_e32 v8, s7, v14
	v_mad_i64_i32 v[8:9], s[4:5], v8, s95, v[4:5]
	v_lshl_add_u64 v[8:9], v[8:9], 0, s[0:1]
	v_lshl_add_u64 v[12:13], v[8:9], 0, v[96:97]
	global_load_dwordx4 v[56:59], v[12:13], off offset:3072
	v_add_co_u32_e32 v8, vcc, s63, v12
	s_nop 1
	v_addc_co_u32_e32 v9, vcc, 0, v13, vcc
	global_load_dwordx4 v[60:63], v[8:9], off
	v_mad_u32_u24 v75, v14, s11, v2
	v_and_b32_e32 v8, -8, v14
	v_ashrrev_i32_e32 v9, 31, v8
	v_lshl_add_u64 v[10:11], v[8:9], 1, v[0:1]
	global_load_dwordx4 v[68:71], v[10:11], off
	v_mul_lo_u32 v8, v8, s11
	v_add_u32_e32 v79, v7, v8
	v_lshlrev_b32_e32 v17, 2, v3
	s_movk_i32 s0, 0x60
	v_lshlrev_b32_e32 v96, 4, v3
	v_add_u32_e32 v18, 0, v96
	v_mad_u32_u24 v19, v16, s11, v18
	v_lshrrev_b32_e32 v0, 1, v143
	v_and_or_b32 v146, v0, s0, v16
	v_mad_u32_u24 v0, v146, s11, v18
	s_waitcnt vmcnt(11)
	ds_write_b128 v72, v[20:23]
	s_waitcnt vmcnt(10)
	ds_write_b128 v72, v[24:27] offset:34816
	s_waitcnt vmcnt(9)
	ds_write_b16 v76, v28
	ds_write_b16_d16_hi v76, v28 offset:272
	ds_write_b16 v76, v29 offset:544
	ds_write_b16_d16_hi v76, v29 offset:816
	ds_write_b16 v76, v30 offset:1088
	ds_write_b16_d16_hi v76, v30 offset:1360
	ds_write_b16 v76, v31 offset:1632
	ds_write_b16_d16_hi v76, v31 offset:1904
	s_waitcnt vmcnt(8)
	ds_write_b128 v73, v[32:35]
	s_waitcnt vmcnt(7)
	ds_write_b128 v73, v[36:39] offset:34816
	s_waitcnt vmcnt(6)
	ds_write_b16 v77, v40
	ds_write_b16_d16_hi v77, v40 offset:272
	ds_write_b16 v77, v41 offset:544
	ds_write_b16_d16_hi v77, v41 offset:816
	ds_write_b16 v77, v42 offset:1088
	ds_write_b16_d16_hi v77, v42 offset:1360
	ds_write_b16 v77, v43 offset:1632
	ds_write_b16_d16_hi v77, v43 offset:1904
	s_waitcnt vmcnt(5)
	ds_write_b128 v74, v[44:47]
	s_waitcnt vmcnt(4)
	ds_write_b128 v74, v[48:51] offset:34816
	s_waitcnt vmcnt(3)
	ds_write_b16 v78, v52
	ds_write_b16_d16_hi v78, v52 offset:272
	ds_write_b16 v78, v53 offset:544
	ds_write_b16_d16_hi v78, v53 offset:816
	ds_write_b16 v78, v54 offset:1088
	ds_write_b16_d16_hi v78, v54 offset:1360
	ds_write_b16 v78, v55 offset:1632
	ds_write_b16_d16_hi v78, v55 offset:1904
	s_waitcnt vmcnt(2)
	ds_write_b128 v75, v[56:59]
	s_waitcnt vmcnt(1)
	ds_write_b128 v75, v[60:63] offset:34816
	s_waitcnt vmcnt(0)
	ds_write_b16 v79, v68
	ds_write_b16_d16_hi v79, v68 offset:272
	ds_write_b16 v79, v69 offset:544
	ds_write_b16_d16_hi v79, v69 offset:816
	ds_write_b16 v79, v70 offset:1088
	ds_write_b16_d16_hi v79, v70 offset:1360
	ds_write_b16 v79, v71 offset:1632
	ds_write_b16_d16_hi v79, v71 offset:1904
	s_waitcnt lgkmcnt(0)
	s_barrier
	ds_read_b128 v[64:67], v0
	ds_read_b128 v[106:109], v0 offset:32
	ds_read_b128 v[102:105], v0 offset:64
	ds_read_b128 v[92:95], v0 offset:96
	ds_read_b128 v[88:91], v0 offset:128
	ds_read_b128 v[84:87], v0 offset:160
	ds_read_b128 v[80:83], v0 offset:192
	ds_read_b128 v[98:101], v0 offset:224
	ds_read_b128 v[0:3], v19 offset:34816
	ds_read_b128 v[20:23], v19 offset:34848
	s_waitcnt lgkmcnt(1)
	v_mfma_f32_32x32x16_bf16 v[0:15], v[0:3], v[64:67], 0
	s_waitcnt lgkmcnt(0)
	v_mfma_f32_32x32x16_bf16 v[0:15], v[20:23], v[106:109], v[0:15]
	ds_read_b128 v[20:23], v19 offset:34880
	s_waitcnt lgkmcnt(0)
	v_mfma_f32_32x32x16_bf16 v[0:15], v[20:23], v[102:105], v[0:15]
	ds_read_b128 v[20:23], v19 offset:34912
	s_waitcnt lgkmcnt(0)
	v_mfma_f32_32x32x16_bf16 v[0:15], v[20:23], v[92:95], v[0:15]
	ds_read_b128 v[20:23], v19 offset:34944
	s_waitcnt lgkmcnt(0)
	v_mfma_f32_32x32x16_bf16 v[0:15], v[20:23], v[88:91], v[0:15]
	ds_read_b128 v[20:23], v19 offset:34976
	s_waitcnt lgkmcnt(0)
	v_mfma_f32_32x32x16_bf16 v[0:15], v[20:23], v[84:87], v[0:15]
	ds_read_b128 v[20:23], v19 offset:35008
	s_waitcnt lgkmcnt(0)
	v_mfma_f32_32x32x16_bf16 v[0:15], v[20:23], v[80:83], v[0:15]
	ds_read_b128 v[20:23], v19 offset:35040
	s_waitcnt lgkmcnt(0)
	v_mfma_f32_32x32x16_bf16 v[0:15], v[20:23], v[98:101], v[0:15]
	v_sub_u32_e32 v20, v146, v17
	v_cmp_gt_i32_e32 vcc, 1, v20
	s_and_saveexec_b64 s[4:5], vcc
	s_xor_b64 s[4:5], exec, s[4:5]
	s_cbranch_execz .LBB0_1042
	v_sub_u32_e32 v19, 0, v20
	v_cvt_f32_u32_e32 v19, v19
	v_cmp_ne_u32_e32 vcc, v146, v17
	v_mul_f32_e32 v19, v144, v19
	v_exp_f32_e32 v19, v19
	s_nop 0
	v_cndmask_b32_e32 v19, 2.0, v19, vcc
